# write-through stores for HID (SwiGLU epilogue) as well
# baseline (speedup 1.0000x reference)
; template <bool BF> __device__ __forceinline__ unsigned pk16(float lo, float hi) { return BF ? pkb(lo, hi) : pkh(lo, hi); }
;     __device__ __forceinline__ void operator()(const Acc& acc, const Unit& u, int wr, int wc, int fr, int fq) const {
;         const int row0 = u.pm * BM + wr * 64 + fr, col0 = u.pn * HALF + wc * 32 + 8 * fq;
;         f16* Og = O + (size_t)u.g * EROWS * DE;
; #pragma unroll
;         for (int ai = 0; ai < 2; ++ai)
; #pragma unroll
;             for (int m = 0; m < 4; ++m) { f16* rowp = Og + (size_t)(row0 + ai * HALF + m * 16) * DE + col0;
;                 float h[8];
; #pragma unroll
;                 for (int n = 0; n < 2; ++n)
; #pragma unroll
;                     for (int j = 0; j < 4; ++j) { const float g = acc[ai][0][m][n][j], up = acc[ai][1][m][n][j]; h[n * 4 + j] = g * up * __builtin_amdgcn_rcpf(1.f + __builtin_amdgcn_exp2f(-LOG2E * g)); }
;                 u32x4 w; w.x = pk16<MOE_BF16>(h[0], h[1]); w.y = pk16<MOE_BF16>(h[2], h[3]); w.z = pk16<MOE_BF16>(h[4], h[5]); w.w = pk16<MOE_BF16>(h[6], h[7]);
;                 *(u32x4*)rowp = w; }
.LBB0_1014:
	v_mul_f32_e32 v141, 0xbfb8aa3b, v98
	v_exp_f32_e32 v141, v141
	v_mul_f32_e32 v145, 0xbfb8aa3b, v99
	v_exp_f32_e32 v145, v145
	v_pk_mul_f32 v[166:167], v[98:99], v[66:67]
	v_add_f32_e32 v141, 1.0, v141
	v_rcp_f32_e32 v150, v141
	v_add_f32_e32 v141, 1.0, v145
	v_rcp_f32_e32 v151, v141
	v_mul_f32_e32 v141, 0xbfb8aa3b, v100
	v_exp_f32_e32 v141, v141
	v_mul_f32_e32 v145, 0xbfb8aa3b, v101
	v_exp_f32_e32 v145, v145
	v_pk_mul_f32 v[150:151], v[150:151], v[166:167]
	v_add_f32_e32 v141, 1.0, v141
	v_rcp_f32_e32 v166, v141
	v_add_f32_e32 v141, 1.0, v145
	v_rcp_f32_e32 v167, v141
	v_mul_f32_e32 v141, 0xbfb8aa3b, v94
	v_exp_f32_e32 v141, v141
	v_mul_f32_e32 v145, 0xbfb8aa3b, v95
	v_exp_f32_e32 v145, v145
	v_pk_mul_f32 v[164:165], v[100:101], v[68:69]
	v_add_f32_e32 v141, 1.0, v141
	v_pk_mul_f32 v[166:167], v[166:167], v[164:165]
	v_rcp_f32_e32 v164, v141
	v_add_f32_e32 v141, 1.0, v145
	v_mul_f32_e32 v145, 0xbfb8aa3b, v96
	v_exp_f32_e32 v145, v145
	v_mul_f32_e32 v163, 0xbfb8aa3b, v97
	v_exp_f32_e32 v163, v163
	v_rcp_f32_e32 v165, v141
	v_add_f32_e32 v141, 1.0, v145
	v_rcp_f32_e32 v168, v141
	v_add_f32_e32 v141, 1.0, v163
	v_rcp_f32_e32 v169, v141
	v_mul_f32_e32 v141, 0xbfb8aa3b, v90
	v_exp_f32_e32 v141, v141
	v_mul_f32_e32 v145, 0xbfb8aa3b, v91
	v_exp_f32_e32 v145, v145
	v_pk_mul_f32 v[172:173], v[94:95], v[62:63]
	v_add_f32_e32 v141, 1.0, v141
	s_add_u32 s2, s21, 0xffffff00
	v_pk_mul_f32 v[172:173], v[164:165], v[172:173]
	v_cvt_pk_bf16_f32 v164, v150, v151
	v_rcp_f32_e32 v150, v141
	v_add_f32_e32 v141, 1.0, v145
	s_addc_u32 s3, s42, -1
	s_mul_i32 s22, s26, 0x1600000
	v_rcp_f32_e32 v151, v141
	v_mul_f32_e32 v141, 0xbfb8aa3b, v92
	v_lshl_or_b32 v148, s10, 7, v143
	s_mul_hi_i32 s21, s26, 0x1600000
	s_add_u32 s22, s76, s22
	v_exp_f32_e32 v141, v141
	v_mul_f32_e32 v145, 0xbfb8aa3b, v93
	s_addc_u32 s23, s77, s21
	v_ashrrev_i32_e32 v149, 31, v148
	v_pk_mul_f32 v[170:171], v[96:97], v[64:65]
	v_exp_f32_e32 v145, v145
	v_lshl_add_u32 v134, s27, 8, v155
	v_lshl_add_u64 v[148:149], v[148:149], 1, s[22:23]
	v_pk_mul_f32 v[168:169], v[168:169], v[170:171]
	v_mad_i64_i32 v[170:171], s[22:23], v134, s37, v[148:149]
	v_cvt_pk_bf16_f32 v165, v166, v167
	v_cvt_pk_bf16_f32 v166, v172, v173
	v_cvt_pk_bf16_f32 v167, v168, v169
	global_store_dwordx4 v[170:171], v[164:167], off sc0 sc1
	v_add_f32_e32 v141, 1.0, v141
	v_pk_mul_f32 v[172:173], v[86:87], v[54:55]
	v_pk_mul_f32 v[166:167], v[90:91], v[58:59]
	v_pk_mul_f32 v[164:165], v[92:93], v[60:61]
	v_pk_mul_f32 v[150:151], v[150:151], v[166:167]
	v_rcp_f32_e32 v166, v141
	v_add_f32_e32 v141, 1.0, v145
	v_rcp_f32_e32 v167, v141
	v_mul_f32_e32 v141, 0xbfb8aa3b, v86
	v_exp_f32_e32 v141, v141
	v_mul_f32_e32 v145, 0xbfb8aa3b, v87
	v_exp_f32_e32 v145, v145
	v_pk_mul_f32 v[166:167], v[166:167], v[164:165]
	v_add_f32_e32 v141, 1.0, v141
	v_rcp_f32_e32 v164, v141
	v_add_f32_e32 v141, 1.0, v145
	v_mul_f32_e32 v145, 0xbfb8aa3b, v88
	v_exp_f32_e32 v145, v145
	v_mul_f32_e32 v165, 0xbfb8aa3b, v89
	v_exp_f32_e32 v169, v165
	v_rcp_f32_e32 v165, v141
	v_add_f32_e32 v141, 1.0, v145
	v_rcp_f32_e32 v168, v141
	v_add_f32_e32 v141, 1.0, v169
	v_rcp_f32_e32 v169, v141
	v_mul_f32_e32 v141, 0xbfb8aa3b, v82
	v_exp_f32_e32 v141, v141
	v_mul_f32_e32 v145, 0xbfb8aa3b, v83
	v_exp_f32_e32 v145, v145
	v_pk_mul_f32 v[172:173], v[164:165], v[172:173]
	v_add_f32_e32 v141, 1.0, v141
	v_cvt_pk_bf16_f32 v164, v150, v151
	v_rcp_f32_e32 v150, v141
	v_add_f32_e32 v141, 1.0, v145
	v_rcp_f32_e32 v151, v141
	v_mul_f32_e32 v141, 0xbfb8aa3b, v84
	v_exp_f32_e32 v141, v141
	v_mul_f32_e32 v145, 0xbfb8aa3b, v85
	v_pk_mul_f32 v[170:171], v[88:89], v[56:57]
	v_exp_f32_e32 v145, v145
	v_or_b32_e32 v163, 16, v134
	v_pk_mul_f32 v[168:169], v[168:169], v[170:171]
	v_mad_i64_i32 v[170:171], s[22:23], v163, s37, v[148:149]
	v_cvt_pk_bf16_f32 v165, v166, v167
	v_cvt_pk_bf16_f32 v166, v172, v173
	v_cvt_pk_bf16_f32 v167, v168, v169
	global_store_dwordx4 v[170:171], v[164:167], off sc0 sc1
	v_add_f32_e32 v141, 1.0, v141
	v_pk_mul_f32 v[172:173], v[78:79], v[46:47]
	v_pk_mul_f32 v[166:167], v[82:83], v[50:51]
	v_pk_mul_f32 v[164:165], v[84:85], v[52:53]
	v_pk_mul_f32 v[150:151], v[150:151], v[166:167]
	v_rcp_f32_e32 v166, v141
	v_add_f32_e32 v141, 1.0, v145
	v_rcp_f32_e32 v167, v141
	v_mul_f32_e32 v141, 0xbfb8aa3b, v78
	v_exp_f32_e32 v141, v141
	v_mul_f32_e32 v145, 0xbfb8aa3b, v79
	v_exp_f32_e32 v145, v145
	v_pk_mul_f32 v[166:167], v[166:167], v[164:165]
	v_add_f32_e32 v141, 1.0, v141
	v_rcp_f32_e32 v164, v141
	v_add_f32_e32 v141, 1.0, v145
	v_mul_f32_e32 v145, 0xbfb8aa3b, v80
	v_exp_f32_e32 v145, v145
	v_mul_f32_e32 v165, 0xbfb8aa3b, v81
	v_exp_f32_e32 v169, v165
	v_rcp_f32_e32 v165, v141
	v_add_f32_e32 v141, 1.0, v145
	v_rcp_f32_e32 v168, v141
	v_add_f32_e32 v141, 1.0, v169
	v_rcp_f32_e32 v169, v141
	v_mul_f32_e32 v141, 0xbfb8aa3b, v74
	v_exp_f32_e32 v141, v141
	v_mul_f32_e32 v145, 0xbfb8aa3b, v75
	v_exp_f32_e32 v145, v145
	v_pk_mul_f32 v[172:173], v[164:165], v[172:173]
	v_add_f32_e32 v141, 1.0, v141
	v_cvt_pk_bf16_f32 v164, v150, v151
	v_rcp_f32_e32 v150, v141
	v_add_f32_e32 v141, 1.0, v145
	v_rcp_f32_e32 v151, v141
	v_mul_f32_e32 v141, 0xbfb8aa3b, v76
	v_exp_f32_e32 v141, v141
	v_mul_f32_e32 v145, 0xbfb8aa3b, v77
	v_pk_mul_f32 v[170:171], v[80:81], v[48:49]
	v_exp_f32_e32 v145, v145
	v_or_b32_e32 v163, 32, v134
	v_pk_mul_f32 v[168:169], v[168:169], v[170:171]
	v_mad_i64_i32 v[170:171], s[22:23], v163, s37, v[148:149]
	v_cvt_pk_bf16_f32 v165, v166, v167
	v_cvt_pk_bf16_f32 v166, v172, v173
	v_cvt_pk_bf16_f32 v167, v168, v169
	global_store_dwordx4 v[170:171], v[164:167], off sc0 sc1
	v_add_f32_e32 v141, 1.0, v141
	v_pk_mul_f32 v[172:173], v[70:71], v[38:39]
; template <bool BF> __device__ __forceinline__ unsigned pk16(float lo, float hi) { return BF ? pkb(lo, hi) : pkh(lo, hi); }
;     __device__ __forceinline__ void operator()(const Acc& acc, const Unit& u, int wr, int wc, int fr, int fq) const {
;         const int row0 = u.pm * BM + wr * 64 + fr, col0 = u.pn * HALF + wc * 32 + 8 * fq;
;         f16* Og = O + (size_t)u.g * EROWS * DE;
; #pragma unroll
;         for (int ai = 0; ai < 2; ++ai)
; #pragma unroll
;             for (int m = 0; m < 4; ++m) { f16* rowp = Og + (size_t)(row0 + ai * HALF + m * 16) * DE + col0;
;                 float h[8];
; #pragma unroll
;                 for (int n = 0; n < 2; ++n)
; #pragma unroll
;                     for (int j = 0; j < 4; ++j) { const float g = acc[ai][0][m][n][j], up = acc[ai][1][m][n][j]; h[n * 4 + j] = g * up * __builtin_amdgcn_rcpf(1.f + __builtin_amdgcn_exp2f(-LOG2E * g)); }
;                 u32x4 w; w.x = pk16<MOE_BF16>(h[0], h[1]); w.y = pk16<MOE_BF16>(h[2], h[3]); w.z = pk16<MOE_BF16>(h[4], h[5]); w.w = pk16<MOE_BF16>(h[6], h[7]);
;                 *(u32x4*)rowp = w; }
	v_pk_mul_f32 v[166:167], v[74:75], v[42:43]
	v_pk_mul_f32 v[164:165], v[76:77], v[44:45]
	v_pk_mul_f32 v[150:151], v[150:151], v[166:167]
	v_rcp_f32_e32 v166, v141
	v_add_f32_e32 v141, 1.0, v145
	v_rcp_f32_e32 v167, v141
	v_mul_f32_e32 v141, 0xbfb8aa3b, v70
	v_exp_f32_e32 v141, v141
	v_mul_f32_e32 v145, 0xbfb8aa3b, v71
	v_exp_f32_e32 v145, v145
	v_pk_mul_f32 v[166:167], v[166:167], v[164:165]
	v_add_f32_e32 v141, 1.0, v141
	v_rcp_f32_e32 v164, v141
	v_add_f32_e32 v141, 1.0, v145
	v_mul_f32_e32 v145, 0xbfb8aa3b, v72
	v_exp_f32_e32 v145, v145
	v_mul_f32_e32 v165, 0xbfb8aa3b, v73
	v_exp_f32_e32 v169, v165
	v_rcp_f32_e32 v165, v141
	v_add_f32_e32 v141, 1.0, v145
	v_rcp_f32_e32 v168, v141
	v_add_f32_e32 v141, 1.0, v169
	v_rcp_f32_e32 v169, v141
	v_mul_f32_e32 v141, 0xbfb8aa3b, v34
	v_exp_f32_e32 v141, v141
	v_mul_f32_e32 v145, 0xbfb8aa3b, v35
	v_exp_f32_e32 v145, v145
	v_pk_mul_f32 v[172:173], v[164:165], v[172:173]
	v_add_f32_e32 v141, 1.0, v141
	v_cvt_pk_bf16_f32 v164, v150, v151
	v_rcp_f32_e32 v150, v141
	v_add_f32_e32 v141, 1.0, v145
	v_rcp_f32_e32 v151, v141
	v_mul_f32_e32 v141, 0xbfb8aa3b, v36
	v_exp_f32_e32 v141, v141
	v_mul_f32_e32 v145, 0xbfb8aa3b, v37
	v_pk_mul_f32 v[170:171], v[72:73], v[40:41]
	v_exp_f32_e32 v145, v145
	v_or_b32_e32 v163, 48, v134
	v_pk_mul_f32 v[168:169], v[168:169], v[170:171]
	v_mad_i64_i32 v[170:171], s[22:23], v163, s37, v[148:149]
	v_cvt_pk_bf16_f32 v165, v166, v167
	v_cvt_pk_bf16_f32 v166, v172, v173
	v_cvt_pk_bf16_f32 v167, v168, v169
	global_store_dwordx4 v[170:171], v[164:167], off sc0 sc1
	v_add_f32_e32 v141, 1.0, v141
	v_pk_mul_f32 v[172:173], v[30:31], v[102:103]
	v_pk_mul_f32 v[166:167], v[34:35], v[2:3]
	v_pk_mul_f32 v[164:165], v[36:37], v[4:5]
	v_pk_mul_f32 v[150:151], v[150:151], v[166:167]
	v_rcp_f32_e32 v166, v141
	v_add_f32_e32 v141, 1.0, v145
	v_rcp_f32_e32 v167, v141
	v_mul_f32_e32 v141, 0xbfb8aa3b, v30
	v_exp_f32_e32 v141, v141
	v_mul_f32_e32 v145, 0xbfb8aa3b, v31
	v_exp_f32_e32 v145, v145
	v_pk_mul_f32 v[166:167], v[166:167], v[164:165]
	v_add_f32_e32 v141, 1.0, v141
	v_rcp_f32_e32 v164, v141
	v_add_f32_e32 v141, 1.0, v145
	v_mul_f32_e32 v145, 0xbfb8aa3b, v32
	v_exp_f32_e32 v145, v145
	v_mul_f32_e32 v165, 0xbfb8aa3b, v33
	v_exp_f32_e32 v169, v165
	v_rcp_f32_e32 v165, v141
	v_add_f32_e32 v141, 1.0, v145
	v_rcp_f32_e32 v168, v141
	v_add_f32_e32 v141, 1.0, v169
	v_rcp_f32_e32 v169, v141
	v_mul_f32_e32 v141, 0xbfb8aa3b, v26
	v_exp_f32_e32 v141, v141
	v_mul_f32_e32 v145, 0xbfb8aa3b, v27
	v_exp_f32_e32 v145, v145
	v_pk_mul_f32 v[172:173], v[164:165], v[172:173]
	v_add_f32_e32 v141, 1.0, v141
	v_cvt_pk_bf16_f32 v164, v150, v151
	v_rcp_f32_e32 v150, v141
	v_add_f32_e32 v141, 1.0, v145
	v_rcp_f32_e32 v151, v141
	v_mul_f32_e32 v141, 0xbfb8aa3b, v28
	v_exp_f32_e32 v141, v141
	v_mul_f32_e32 v145, 0xbfb8aa3b, v29
	v_pk_mul_f32 v[170:171], v[32:33], v[104:105]
	v_exp_f32_e32 v145, v145
	v_add_u32_e32 v163, 0x80, v134
	v_pk_mul_f32 v[168:169], v[168:169], v[170:171]
	v_mad_i64_i32 v[170:171], s[22:23], v163, s37, v[148:149]
	v_cvt_pk_bf16_f32 v165, v166, v167
	v_cvt_pk_bf16_f32 v166, v172, v173
	v_cvt_pk_bf16_f32 v167, v168, v169
	global_store_dwordx4 v[170:171], v[164:167], off sc0 sc1
	v_add_f32_e32 v141, 1.0, v141
	v_pk_mul_f32 v[172:173], v[22:23], v[110:111]
	v_pk_mul_f32 v[166:167], v[26:27], v[106:107]
	v_pk_mul_f32 v[164:165], v[28:29], v[108:109]
	v_pk_mul_f32 v[150:151], v[150:151], v[166:167]
	v_rcp_f32_e32 v166, v141
	v_add_f32_e32 v141, 1.0, v145
	v_rcp_f32_e32 v167, v141
	v_mul_f32_e32 v141, 0xbfb8aa3b, v22
	v_exp_f32_e32 v141, v141
	v_mul_f32_e32 v145, 0xbfb8aa3b, v23
	v_exp_f32_e32 v145, v145
	v_pk_mul_f32 v[166:167], v[166:167], v[164:165]
	v_add_f32_e32 v141, 1.0, v141
	v_rcp_f32_e32 v164, v141
	v_add_f32_e32 v141, 1.0, v145
	v_mul_f32_e32 v145, 0xbfb8aa3b, v24
	v_exp_f32_e32 v145, v145
	v_mul_f32_e32 v165, 0xbfb8aa3b, v25
	v_exp_f32_e32 v169, v165
	v_rcp_f32_e32 v165, v141
	v_add_f32_e32 v141, 1.0, v145
; template <bool BF> __device__ __forceinline__ unsigned pk16(float lo, float hi) { return BF ? pkb(lo, hi) : pkh(lo, hi); }
;     __device__ __forceinline__ void operator()(const Acc& acc, const Unit& u, int wr, int wc, int fr, int fq) const {
;         const int row0 = u.pm * BM + wr * 64 + fr, col0 = u.pn * HALF + wc * 32 + 8 * fq;
;         f16* Og = O + (size_t)u.g * EROWS * DE;
; #pragma unroll
;         for (int ai = 0; ai < 2; ++ai)
; #pragma unroll
;             for (int m = 0; m < 4; ++m) { f16* rowp = Og + (size_t)(row0 + ai * HALF + m * 16) * DE + col0;
;                 float h[8];
; #pragma unroll
;                 for (int n = 0; n < 2; ++n)
; #pragma unroll
;                     for (int j = 0; j < 4; ++j) { const float g = acc[ai][0][m][n][j], up = acc[ai][1][m][n][j]; h[n * 4 + j] = g * up * __builtin_amdgcn_rcpf(1.f + __builtin_amdgcn_exp2f(-LOG2E * g)); }
;                 u32x4 w; w.x = pk16<MOE_BF16>(h[0], h[1]); w.y = pk16<MOE_BF16>(h[2], h[3]); w.z = pk16<MOE_BF16>(h[4], h[5]); w.w = pk16<MOE_BF16>(h[6], h[7]);
;                 *(u32x4*)rowp = w; }
	v_rcp_f32_e32 v168, v141
	v_add_f32_e32 v141, 1.0, v169
	v_rcp_f32_e32 v169, v141
	v_mul_f32_e32 v141, 0xbfb8aa3b, v18
	v_exp_f32_e32 v141, v141
	v_mul_f32_e32 v145, 0xbfb8aa3b, v19
	v_exp_f32_e32 v145, v145
	v_pk_mul_f32 v[172:173], v[164:165], v[172:173]
	v_add_f32_e32 v141, 1.0, v141
	v_cvt_pk_bf16_f32 v164, v150, v151
	v_rcp_f32_e32 v150, v141
	v_add_f32_e32 v141, 1.0, v145
	v_rcp_f32_e32 v151, v141
	v_mul_f32_e32 v141, 0xbfb8aa3b, v20
	v_exp_f32_e32 v141, v141
	v_mul_f32_e32 v145, 0xbfb8aa3b, v21
	v_pk_mul_f32 v[170:171], v[24:25], v[112:113]
	v_exp_f32_e32 v145, v145
	v_add_u32_e32 v163, 0x90, v134
	v_pk_mul_f32 v[168:169], v[168:169], v[170:171]
	v_mad_i64_i32 v[170:171], s[22:23], v163, s37, v[148:149]
	v_cvt_pk_bf16_f32 v165, v166, v167
	v_cvt_pk_bf16_f32 v166, v172, v173
	v_cvt_pk_bf16_f32 v167, v168, v169
	global_store_dwordx4 v[170:171], v[164:167], off sc0 sc1
	v_add_f32_e32 v141, 1.0, v141
	v_pk_mul_f32 v[172:173], v[14:15], v[118:119]
	v_pk_mul_f32 v[166:167], v[18:19], v[114:115]
	v_pk_mul_f32 v[164:165], v[20:21], v[116:117]
	v_pk_mul_f32 v[150:151], v[150:151], v[166:167]
	v_rcp_f32_e32 v166, v141
	v_add_f32_e32 v141, 1.0, v145
	v_rcp_f32_e32 v167, v141
	v_mul_f32_e32 v141, 0xbfb8aa3b, v14
	v_exp_f32_e32 v141, v141
	v_mul_f32_e32 v145, 0xbfb8aa3b, v15
	v_exp_f32_e32 v145, v145
	v_pk_mul_f32 v[166:167], v[166:167], v[164:165]
	v_add_f32_e32 v141, 1.0, v141
	v_rcp_f32_e32 v164, v141
	v_add_f32_e32 v141, 1.0, v145
	v_mul_f32_e32 v145, 0xbfb8aa3b, v16
	v_exp_f32_e32 v145, v145
	v_mul_f32_e32 v165, 0xbfb8aa3b, v17
	v_exp_f32_e32 v169, v165
	v_rcp_f32_e32 v165, v141
	v_add_f32_e32 v141, 1.0, v145
	v_rcp_f32_e32 v168, v141
	v_add_f32_e32 v141, 1.0, v169
	v_rcp_f32_e32 v169, v141
	v_mul_f32_e32 v141, 0xbfb8aa3b, v10
	v_exp_f32_e32 v141, v141
	v_mul_f32_e32 v145, 0xbfb8aa3b, v11
	v_exp_f32_e32 v145, v145
	v_pk_mul_f32 v[172:173], v[164:165], v[172:173]
	v_add_f32_e32 v141, 1.0, v141
	v_cvt_pk_bf16_f32 v164, v150, v151
	v_rcp_f32_e32 v150, v141
	v_add_f32_e32 v141, 1.0, v145
	v_rcp_f32_e32 v151, v141
	v_mul_f32_e32 v141, 0xbfb8aa3b, v12
	v_exp_f32_e32 v141, v141
	v_mul_f32_e32 v145, 0xbfb8aa3b, v13
	v_pk_mul_f32 v[170:171], v[16:17], v[120:121]
	v_exp_f32_e32 v145, v145
	v_add_u32_e32 v163, 0xa0, v134
	v_pk_mul_f32 v[168:169], v[168:169], v[170:171]
	v_mad_i64_i32 v[170:171], s[22:23], v163, s37, v[148:149]
	v_cvt_pk_bf16_f32 v165, v166, v167
	v_cvt_pk_bf16_f32 v166, v172, v173
	v_cvt_pk_bf16_f32 v167, v168, v169
	global_store_dwordx4 v[170:171], v[164:167], off sc0 sc1
	v_add_f32_e32 v141, 1.0, v141
	v_mul_f32_e32 v163, 0xbfb8aa3b, v9
	v_pk_mul_f32 v[166:167], v[10:11], v[122:123]
	v_pk_mul_f32 v[164:165], v[12:13], v[124:125]
	v_pk_mul_f32 v[150:151], v[150:151], v[166:167]
	v_rcp_f32_e32 v166, v141
	v_add_f32_e32 v141, 1.0, v145
	v_rcp_f32_e32 v167, v141
	v_mul_f32_e32 v141, 0xbfb8aa3b, v6
	v_exp_f32_e32 v141, v141
	v_mul_f32_e32 v145, 0xbfb8aa3b, v7
	v_exp_f32_e32 v145, v145
	v_pk_mul_f32 v[164:165], v[166:167], v[164:165]
	v_add_f32_e32 v141, 1.0, v141
	v_rcp_f32_e32 v166, v141
	v_add_f32_e32 v141, 1.0, v145
	v_mul_f32_e32 v145, 0xbfb8aa3b, v8
	v_exp_f32_e32 v145, v145
	v_exp_f32_e32 v163, v163
	v_rcp_f32_e32 v167, v141
	v_pk_mul_f32 v[170:171], v[8:9], v[128:129]
	v_add_f32_e32 v141, 1.0, v145
	v_rcp_f32_e32 v168, v141
	v_add_f32_e32 v141, 1.0, v163
	v_rcp_f32_e32 v169, v141
	v_pk_mul_f32 v[172:173], v[6:7], v[126:127]
	v_add_u32_e32 v134, 0xb0, v134
	v_pk_mul_f32 v[166:167], v[166:167], v[172:173]
	v_pk_mul_f32 v[168:169], v[168:169], v[170:171]
	v_mad_i64_i32 v[170:171], s[22:23], v134, s37, v[148:149]
	v_cvt_pk_bf16_f32 v148, v150, v151
	v_cvt_pk_bf16_f32 v149, v164, v165
	v_cvt_pk_bf16_f32 v150, v166, v167
	v_cvt_pk_bf16_f32 v151, v168, v169
	s_and_b64 vcc, exec, s[6:7]
	global_store_dwordx4 v[170:171], v[148:151], off sc0 sc1
	s_cbranch_vccnz .LBB0_1017
	s_andn2_b64 vcc, exec, s[12:13]
	s_cbranch_vccnz .LBB0_1003
	s_barrier
	s_branch .LBB0_1003
